# rowpass router: 4-step lgkmcnt ladders collapsed to one wait per 4 ds_reads (90 fewer s_waitcnt per row)
# speedup vs baseline: 1.0104x; 1.0104x over previous
; DI float bflo(unsigned w) { return __uint_as_float(w << 16); }
; DI float bfhi(unsigned w) { return __uint_as_float(w & 0xffff0000u); }
; DI unsigned pk2(float lo, float hi) { unsigned r; asm("v_cvt_pk_bf16_f32 %0, %1, %2" : "=v"(r) : "v"(lo), "v"(hi)); return r; }
; DI void ph_rowpass(const Frame& F) {
;     ...
;       for (int m = blk * 64 + F.wave * 8; m < blk * 64 + F.wave * 8 + 8; ++m) {
;         const int b = m >> 12, s = m & 4095;
;         const u32x2* mr = (const u32x2*)(MIX + (size_t)m * D) + F.lane;
;         f32x4 v[8]; float ss = 0.f;
; #pragma unroll
;         for (int j = 0; j < 8; ++j) { const u32x2 w = __builtin_nontemporal_load(mr + 64 * j); v[j] = (f32x4){bflo(w.x), bfhi(w.x), bflo(w.y), bfhi(w.y)}; ss += (v[j][0] * v[j][0] + v[j][1] * v[j][1]) + (v[j][2] * v[j][2] + v[j][3] * v[j][3]); }
;         const f32x4* xr = (const f32x4*)(x + (size_t)m * D) + F.lane;
;         f32x4 xc[8];
; #pragma unroll
;         for (int j = 0; j < 8; ++j) xc[j] = __builtin_nontemporal_load(xr + 64 * j);
;         const float rstd = rsqrtf(wave_sum(ss) * (1.f / D) + NORM_EPS);
;         u32x2* x1r = (u32x2*)(X1 + (size_t)m * D) + F.lane;
;         float ss2 = 0.f;
; #pragma unroll
;         for (int j = 0; j < 8; ++j) {
;             const f32x4 gg = pgm[F.lane + 64 * j], xv = xc[j];
; #pragma unroll
;             for (int i = 0; i < 4; ++i) v[j][i] = xv[i] + (v[j][i] * rstd) * gg[i];
;             x1r[64 * j] = (u32x2){pk2(v[j][0], v[j][1]), pk2(v[j][2], v[j][3])};
;             ss2 += (v[j][0] * v[j][0] + v[j][1] * v[j][1]) + (v[j][2] * v[j][2] + v[j][3] * v[j][3]);
;         }
;         const float rstd2 = rsqrtf(wave_sum(ss2) * (1.f / D) + NORM_EPS);
.LBB4_1123:
	v_lshl_add_u64 v[12:13], s[46:47], 0, v[62:63]
	v_lshl_add_u64 v[26:27], v[60:61], 0, s[20:21]
	s_waitcnt vmcnt(1)
	v_mov_b64_e32 v[8:9], v[218:219]
	v_mov_b64_e32 v[10:11], v[220:221]
	v_mov_b64_e32 v[14:15], v[222:223]
	v_mov_b64_e32 v[16:17], v[224:225]
	v_mov_b64_e32 v[18:19], v[226:227]
	v_mov_b64_e32 v[20:21], v[228:229]
	v_mov_b64_e32 v[22:23], v[230:231]
	v_mov_b64_e32 v[24:25], v[232:233]
	v_mov_b64_e32 v[32:33], v[234:235]
	v_mov_b64_e32 v[34:35], v[236:237]
	v_mov_b64_e32 v[4:5], v[238:239]
	v_mov_b64_e32 v[6:7], v[240:241]
	v_mov_b64_e32 v[0:1], v[242:243]
	v_mov_b64_e32 v[2:3], v[244:245]
	v_mov_b64_e32 v[28:29], v[246:247]
	v_mov_b64_e32 v[30:31], v[248:249]
	s_waitcnt vmcnt(11)
	v_and_b32_e32 v66, 0xffff0000, v8
	v_and_b32_e32 v70, 0xffff0000, v9
	s_waitcnt vmcnt(10)
	v_and_b32_e32 v158, 0xffff0000, v10
	v_and_b32_e32 v160, 0xffff0000, v11
	v_lshlrev_b32_e32 v64, 16, v8
	v_lshlrev_b32_e32 v68, 16, v9
	v_lshlrev_b32_e32 v153, 16, v10
	v_lshlrev_b32_e32 v159, 16, v11
	s_waitcnt vmcnt(9)
	v_and_b32_e32 v162, 0xffff0000, v14
	v_and_b32_e32 v164, 0xffff0000, v15
	v_mul_f32_e32 v8, v66, v66
	v_mul_f32_e32 v9, v70, v70
	v_mul_f32_e32 v10, v158, v158
	v_mul_f32_e32 v11, v160, v160
	v_lshlrev_b32_e32 v161, 16, v14
	v_lshlrev_b32_e32 v163, 16, v15
	s_waitcnt vmcnt(8)
	v_and_b32_e32 v166, 0xffff0000, v16
	v_and_b32_e32 v168, 0xffff0000, v17
	v_mul_f32_e32 v14, v162, v162
	v_mul_f32_e32 v15, v164, v164
	v_fmac_f32_e32 v8, v64, v64
	v_fmac_f32_e32 v9, v68, v68
	v_fmac_f32_e32 v10, v153, v153
	v_fmac_f32_e32 v11, v159, v159
	v_lshlrev_b32_e32 v165, 16, v16
	v_lshlrev_b32_e32 v167, 16, v17
	s_waitcnt vmcnt(7)
	v_and_b32_e32 v170, 0xffff0000, v18
	v_and_b32_e32 v172, 0xffff0000, v19
	v_mul_f32_e32 v16, v166, v166
	v_mul_f32_e32 v17, v168, v168
	v_fmac_f32_e32 v14, v161, v161
	v_fmac_f32_e32 v15, v163, v163
	v_add_f32_e32 v8, v8, v9
	v_add_f32_e32 v9, v10, v11
	v_lshlrev_b32_e32 v169, 16, v18
	v_lshlrev_b32_e32 v171, 16, v19
	s_waitcnt vmcnt(6)
	v_and_b32_e32 v174, 0xffff0000, v20
	v_and_b32_e32 v176, 0xffff0000, v21
	v_mul_f32_e32 v18, v170, v170
	v_mul_f32_e32 v19, v172, v172
	v_fmac_f32_e32 v16, v165, v165
	v_fmac_f32_e32 v17, v167, v167
	v_add_f32_e32 v10, v14, v15
	v_add_f32_e32 v8, v8, v9
	v_lshlrev_b32_e32 v173, 16, v20
	v_lshlrev_b32_e32 v175, 16, v21
	s_waitcnt vmcnt(5)
	v_and_b32_e32 v178, 0xffff0000, v22
	v_and_b32_e32 v180, 0xffff0000, v23
	v_mul_f32_e32 v20, v174, v174
	v_mul_f32_e32 v21, v176, v176
	v_fmac_f32_e32 v18, v169, v169
	v_fmac_f32_e32 v19, v171, v171
	v_add_f32_e32 v11, v16, v17
	v_add_f32_e32 v8, v8, v10
	v_lshlrev_b32_e32 v177, 16, v22
	v_lshlrev_b32_e32 v179, 16, v23
	s_waitcnt vmcnt(4)
	v_and_b32_e32 v182, 0xffff0000, v24
	v_and_b32_e32 v184, 0xffff0000, v25
	v_mul_f32_e32 v22, v178, v178
	v_mul_f32_e32 v23, v180, v180
	v_fmac_f32_e32 v20, v173, v173
	v_fmac_f32_e32 v21, v175, v175
	v_add_f32_e32 v14, v18, v19
	v_add_f32_e32 v8, v8, v11
	v_lshlrev_b32_e32 v181, 16, v24
	v_lshlrev_b32_e32 v183, 16, v25
	v_mul_f32_e32 v24, v182, v182
	v_fmac_f32_e32 v22, v177, v177
	v_fmac_f32_e32 v23, v179, v179
	v_add_f32_e32 v15, v20, v21
	v_add_f32_e32 v8, v8, v14
	v_mul_f32_e32 v9, v184, v184
	v_fmac_f32_e32 v24, v181, v181
	v_add_f32_e32 v16, v22, v23
	v_add_f32_e32 v8, v8, v15
	v_fmac_f32_e32 v9, v183, v183
	v_add_f32_e32 v8, v8, v16
	v_add_f32_e32 v9, v24, v9
	v_add_f32_e32 v8, v8, v9
	s_nop 1
	v_add_f32_dpp v8, v8, v8 quad_perm:[1,0,3,2] row_mask:0xf bank_mask:0xf bound_ctrl:1
	s_nop 1
	v_add_f32_dpp v8, v8, v8 quad_perm:[2,3,0,1] row_mask:0xf bank_mask:0xf bound_ctrl:1
	s_nop 1
	v_add_f32_dpp v8, v8, v8 row_half_mirror row_mask:0xf bank_mask:0xf bound_ctrl:1
	s_nop 1
	v_add_f32_dpp v10, v8, v8 row_mirror row_mask:0xf bank_mask:0xf bound_ctrl:1
	v_add_co_u32_e32 v8, vcc, s27, v26
	ds_swizzle_b32 v11, v10 offset:swizzle(SWAP,16)
	s_nop 0
	v_addc_co_u32_e32 v9, vcc, 0, v27, vcc
	global_load_dwordx4 v[22:25], v[8:9], off nt
	global_load_dwordx4 v[18:21], v[8:9], off offset:1024 nt
	s_waitcnt lgkmcnt(0)
	v_add_f32_e32 v10, v10, v11
	v_mov_b32_e32 v11, v10
	s_nop 1
	v_permlane32_swap_b32_e32 v10, v11
	v_add_f32_e32 v10, v10, v11
	v_fmamk_f32 v10, v10, 0x3a000000, v151
	v_mul_f32_e32 v11, 0x4b800000, v10
	v_cmp_gt_f32_e32 vcc, s37, v10
	s_nop 1
	v_cndmask_b32_e32 v10, v10, v11, vcc
	v_rsq_f32_e32 v26, v10
	global_load_dwordx4 v[14:17], v[8:9], off offset:2048 nt
	s_nop 0
	global_load_dwordx4 v[8:11], v[8:9], off offset:3072 nt
	ds_read_b128 v[36:39], v67
	ds_read_b128 v[154:157], v67 offset:1024
	v_mul_f32_e32 v27, 0x45800000, v26
	v_cndmask_b32_e32 v185, v26, v27, vcc
	v_mul_f32_e32 v26, v185, v64
	s_waitcnt vmcnt(7) lgkmcnt(1)
	v_fma_f32 v64, v36, v26, v32
	v_mul_f32_e32 v26, v185, v66
	v_fma_f32 v66, v37, v26, v33
	v_mul_f32_e32 v26, v185, v68
	v_fma_f32 v34, v38, v26, v34
	v_mul_f32_e32 v26, v185, v70
	v_fmac_f32_e32 v35, v39, v26
	v_add_co_u32_e32 v32, vcc, s38, v12
	v_mul_f32_e32 v12, v66, v66
	s_nop 0
	v_addc_co_u32_e32 v33, vcc, 0, v13, vcc
	v_mul_f32_e32 v13, v35, v35
	v_fmac_f32_e32 v12, v64, v64
	v_fmac_f32_e32 v13, v34, v34
	v_add_f32_e32 v12, v12, v13
	v_mul_f32_e32 v13, v185, v153
	s_waitcnt vmcnt(6) lgkmcnt(0)
	v_fma_f32 v153, v154, v13, v4
	v_mul_f32_e32 v4, v185, v158
	v_fma_f32 v186, v155, v4, v5
	v_mul_f32_e32 v4, v185, v159
	v_fma_f32 v6, v156, v4, v6
	v_mul_f32_e32 v4, v185, v160
	ds_read_b128 v[36:39], v67 offset:2048
	v_fmac_f32_e32 v7, v157, v4
	v_cvt_pk_bf16_f32 v4, v153, v186
	v_cvt_pk_bf16_f32 v5, v6, v7
	global_store_dwordx2 v[32:33], v[4:5], off offset:512
	v_mul_f32_e32 v4, v186, v186
	v_mul_f32_e32 v5, v7, v7
	v_fmac_f32_e32 v4, v153, v153
	v_fmac_f32_e32 v5, v6, v6
	v_add_f32_e32 v4, v4, v5
	v_mul_f32_e32 v5, v185, v161
	ds_read_b128 v[154:157], v67 offset:3072
	s_waitcnt vmcnt(6) lgkmcnt(1)
; DI unsigned pk2(float lo, float hi) { unsigned r; asm("v_cvt_pk_bf16_f32 %0, %1, %2" : "=v"(r) : "v"(lo), "v"(hi)); return r; }
; DI void ph_rowpass(const Frame& F) {
;     ...
; #pragma unroll
;         for (int j = 0; j < 8; ++j) {
;             const f32x4 gg = pgm[F.lane + 64 * j], xv = xc[j];
; #pragma unroll
;             for (int i = 0; i < 4; ++i) v[j][i] = xv[i] + (v[j][i] * rstd) * gg[i];
;             x1r[64 * j] = (u32x2){pk2(v[j][0], v[j][1]), pk2(v[j][2], v[j][3])};
;             ss2 += (v[j][0] * v[j][0] + v[j][1] * v[j][1]) + (v[j][2] * v[j][2] + v[j][3] * v[j][3]);
;         }
;         const float rstd2 = rsqrtf(wave_sum(ss2) * (1.f / D) + NORM_EPS);
;         u32x2* h2r = (u32x2*)(H2 + (size_t)m * D) + F.lane;
;         f32x2 lgp[8];
; #pragma unroll
;         for (int e = 0; e < 8; ++e) lgp[e] = (f32x2){0.f, 0.f};
; #pragma unroll
;         for (int j = 0; j < 8; ++j) {
;             const f32x4 gg = pgf[F.lane + 64 * j], sh = psh[F.lane + 64 * j];
;             float h[4];
; #pragma unroll
;             for (int i = 0; i < 4; ++i) h[i] = v[j][i] * rstd2 * gg[i] + sh[i];
;     ...
;             ((unsigned*)((unsigned char*)H2 + (size_t)m * D))[F.lane + 64 * j] = pk4_f8(h[0] * F8_HSCALE, h[1] * F8_HSCALE, h[2] * F8_HSCALE, h[3] * F8_HSCALE);
;     ...
;             h2r[64 * j] = (u32x2){pk2(h[0], h[1]), pk2(h[2], h[3])};
;     ...
; #pragma unroll
;             for (int i = 0; i < 4; ++i) v[j][i] = h[i];
;         }
	v_fma_f32 v160, v36, v5, v0
	v_mul_f32_e32 v0, v185, v162
	v_fma_f32 v161, v37, v0, v1
	v_mul_f32_e32 v0, v185, v163
	v_fma_f32 v2, v38, v0, v2
	v_mul_f32_e32 v0, v185, v164
	v_fmac_f32_e32 v3, v39, v0
	v_cvt_pk_bf16_f32 v0, v160, v161
	v_cvt_pk_bf16_f32 v1, v2, v3
	global_store_dwordx2 v[32:33], v[0:1], off offset:1024
	v_mul_f32_e32 v0, v161, v161
	v_mul_f32_e32 v1, v3, v3
	v_fmac_f32_e32 v0, v160, v160
	v_fmac_f32_e32 v1, v2, v2
	v_add_f32_e32 v4, v12, v4
	v_add_f32_e32 v0, v0, v1
	v_add_f32_e32 v4, v0, v4
	v_mul_f32_e32 v0, v185, v165
	s_waitcnt vmcnt(6) lgkmcnt(0)
	v_fma_f32 v154, v0, v154, v28
	v_mul_f32_e32 v0, v185, v166
	v_fma_f32 v155, v0, v155, v29
	v_mul_f32_e32 v0, v185, v167
	v_cvt_pk_bf16_f32 v26, v64, v66
	v_cvt_pk_bf16_f32 v27, v34, v35
	v_fma_f32 v156, v0, v156, v30
	v_mul_f32_e32 v0, v185, v168
	global_store_dwordx2 v[32:33], v[26:27], off
	v_fmac_f32_e32 v31, v0, v157
	v_cvt_pk_bf16_f32 v0, v154, v155
	v_cvt_pk_bf16_f32 v1, v156, v31
	ds_read_b128 v[26:29], v67 offset:4096
	ds_read_b128 v[36:39], v67 offset:5120
	global_store_dwordx2 v[32:33], v[0:1], off offset:1536
	v_mul_f32_e32 v0, v155, v155
	v_mul_f32_e32 v1, v31, v31
	v_fmac_f32_e32 v0, v154, v154
	v_fmac_f32_e32 v1, v156, v156
	v_add_f32_e32 v0, v0, v1
	v_add_f32_e32 v4, v4, v0
	v_mul_f32_e32 v0, v185, v169
	s_waitcnt vmcnt(7) lgkmcnt(1)
	v_fma_f32 v22, v0, v26, v22
	v_mul_f32_e32 v0, v185, v170
	v_fma_f32 v23, v0, v27, v23
	v_mul_f32_e32 v0, v185, v171
	v_fma_f32 v157, v0, v28, v24
	v_mul_f32_e32 v0, v185, v172
	v_fmac_f32_e32 v25, v0, v29
	v_cvt_pk_bf16_f32 v0, v22, v23
	v_cvt_pk_bf16_f32 v1, v157, v25
	global_store_dwordx2 v[32:33], v[0:1], off offset:2048
	v_mul_f32_e32 v0, v23, v23
	v_mul_f32_e32 v1, v25, v25
	v_fmac_f32_e32 v0, v22, v22
	v_fmac_f32_e32 v1, v157, v157
	v_add_f32_e32 v0, v0, v1
	v_add_f32_e32 v4, v4, v0
	v_mul_f32_e32 v0, v185, v173
	s_waitcnt vmcnt(7) lgkmcnt(0)
	v_fma_f32 v18, v0, v36, v18
	v_mul_f32_e32 v0, v185, v174
	v_fma_f32 v19, v0, v37, v19
	v_mul_f32_e32 v0, v185, v175
	v_fma_f32 v162, v0, v38, v20
	v_mul_f32_e32 v0, v185, v176
	v_fmac_f32_e32 v21, v0, v39
	v_cvt_pk_bf16_f32 v0, v18, v19
	v_cvt_pk_bf16_f32 v1, v162, v21
	ds_read_b128 v[26:29], v67 offset:6144
	ds_read_b128 v[36:39], v67 offset:7168
	global_store_dwordx2 v[32:33], v[0:1], off offset:2560
	v_mul_f32_e32 v0, v19, v19
	v_mul_f32_e32 v1, v21, v21
	v_fmac_f32_e32 v0, v18, v18
	v_fmac_f32_e32 v1, v162, v162
	v_add_f32_e32 v0, v0, v1
	v_add_f32_e32 v1, v4, v0
	v_mul_f32_e32 v0, v185, v177
	s_waitcnt vmcnt(7) lgkmcnt(1)
	v_fma_f32 v163, v0, v26, v14
	v_mul_f32_e32 v0, v185, v178
	v_fma_f32 v164, v0, v27, v15
	v_mul_f32_e32 v0, v185, v179
	v_fma_f32 v165, v0, v28, v16
	v_mul_f32_e32 v0, v185, v180
	v_fmac_f32_e32 v17, v0, v29
	v_mul_f32_e32 v4, v164, v164
	v_mul_f32_e32 v5, v17, v17
	v_fmac_f32_e32 v4, v163, v163
	v_fmac_f32_e32 v5, v165, v165
	v_add_f32_e32 v4, v4, v5
	v_add_f32_e32 v1, v1, v4
	v_mul_f32_e32 v4, v185, v181
	s_waitcnt vmcnt(6) lgkmcnt(0)
	v_fma_f32 v166, v4, v36, v8
	v_mul_f32_e32 v4, v185, v182
	v_fma_f32 v167, v4, v37, v9
	v_mul_f32_e32 v4, v185, v183
	v_fma_f32 v168, v4, v38, v10
	v_mul_f32_e32 v4, v185, v184
	v_fmac_f32_e32 v11, v4, v39
	v_mul_f32_e32 v4, v167, v167
	v_mul_f32_e32 v5, v11, v11
	v_fmac_f32_e32 v4, v166, v166
	v_fmac_f32_e32 v5, v168, v168
	v_add_f32_e32 v4, v4, v5
	v_add_f32_e32 v1, v1, v4
	v_cvt_pk_bf16_f32 v0, v163, v164
	v_mov_b32_e32 v10, 0
	v_mov_b32_e32 v16, 0
	v_add_f32_dpp v1, v1, v1 quad_perm:[1,0,3,2] row_mask:0xf bank_mask:0xf bound_ctrl:1
	s_nop 1
	v_add_f32_dpp v1, v1, v1 quad_perm:[2,3,0,1] row_mask:0xf bank_mask:0xf bound_ctrl:1
	s_nop 1
	v_add_f32_dpp v1, v1, v1 row_half_mirror row_mask:0xf bank_mask:0xf bound_ctrl:1
	s_nop 1
	v_add_f32_dpp v4, v1, v1 row_mirror row_mask:0xf bank_mask:0xf bound_ctrl:1
	ds_swizzle_b32 v5, v4 offset:swizzle(SWAP,16)
	v_cvt_pk_bf16_f32 v1, v165, v17
	global_store_dwordx2 v[32:33], v[0:1], off offset:3072
	ds_read_b128 v[12:15], v69
	ds_read_b128 v[36:39], v71
	v_cvt_pk_bf16_f32 v0, v166, v167
	s_waitcnt lgkmcnt(2)
	v_add_f32_e32 v4, v4, v5
	v_mov_b32_e32 v5, v4
	s_nop 1
	v_permlane32_swap_b32_e32 v4, v5
	v_add_f32_e32 v4, v4, v5
	v_fmamk_f32 v4, v4, 0x3a000000, v151
	v_mul_f32_e32 v5, 0x4b800000, v4
	v_cmp_gt_f32_e32 vcc, s37, v4
	v_cvt_pk_bf16_f32 v1, v168, v11
	global_store_dwordx2 v[32:33], v[0:1], off offset:3584
	s_nop 0
	v_cndmask_b32_e32 v4, v4, v5, vcc
	v_rsq_f32_e32 v4, v4
	v_mov_b32_e32 v5, 0
	v_mul_f32_e32 v0, 0x45800000, v4
	v_cndmask_b32_e32 v169, v4, v0, vcc
	v_mul_f32_e32 v0, v64, v169
	s_waitcnt lgkmcnt(0)
	v_fma_f32 v202, v12, v0, v36
	v_mul_f32_e32 v0, v66, v169
	v_fma_f32 v70, v13, v0, v37
	v_mul_f32_e32 v0, v34, v169
	v_fma_f32 v68, v14, v0, v38
	v_mul_f32_e32 v0, v35, v169
	v_fmac_f32_e32 v39, v15, v0
	v_mul_f32_e32 v0, 0x41000000, v202
	v_mul_f32_e32 v1, 0x41000000, v70
	v_med3_f32 v0, v0, s39, v152
	v_med3_f32 v1, v1, s39, v152
	v_cvt_pk_fp8_f32 v5, v0, v1
	ds_read_b128 v[12:15], v72
	ds_read_b128 v[32:35], v73
	v_mul_f32_e32 v4, 0x41000000, v68
	v_mul_f32_e32 v0, 0x41000000, v39
	v_med3_f32 v1, v4, s39, v152
	v_med3_f32 v0, v0, s39, v152
	v_cvt_pk_fp8_f32 v5, v1, v0 op_sel:[0,0,1]
	v_lshl_add_u64 v[0:1], s[46:47], 0, v[58:59]
	v_add_co_u32_e32 v158, vcc, s40, v0
	v_mul_f32_e32 v0, v153, v169
	s_waitcnt lgkmcnt(0)
; DI unsigned pk2(float lo, float hi) { unsigned r; asm("v_cvt_pk_bf16_f32 %0, %1, %2" : "=v"(r) : "v"(lo), "v"(hi)); return r; }
; #define RT_LD(W, t_) do { _Pragma("unroll") for (int q = 0; q < 4; ++q) W[q] = wl[((((t_)) * 4 + q) << 6) + F.lane]; } while (0)
; #define RT_FMA(W, t_) do { const float hv_ = v[(t_) >> 2][(t_) & 3]; const f32x2 hh = {hv_, hv_}; _Pragma("unroll") for (int q = 0; q < 4; ++q) { \
;                 lgp[2 * q] = __builtin_elementwise_fma(hh, (f32x2){W[q][0], W[q][1]}, lgp[2 * q]); lgp[2 * q + 1] = __builtin_elementwise_fma(hh, (f32x2){W[q][2], W[q][3]}, lgp[2 * q + 1]); } \
;                 asm volatile("" ::: "memory"); } while (0)
; DI void ph_rowpass(const Frame& F) {
;     ...
;             for (int i = 0; i < 4; ++i) h[i] = v[j][i] * rstd2 * gg[i] + sh[i];
;     ...
;             ((unsigned*)((unsigned char*)H2 + (size_t)m * D))[F.lane + 64 * j] = pk4_f8(h[0] * F8_HSCALE, h[1] * F8_HSCALE, h[2] * F8_HSCALE, h[3] * F8_HSCALE);
;     ...
;             h2r[64 * j] = (u32x2){pk2(h[0], h[1]), pk2(h[2], h[3])};
;     ...
; #pragma unroll
;             for (int i = 0; i < 4; ++i) v[j][i] = h[i];
;         }
;         {
;             f32x4 wq0[4], wq1[4], wq2[4];
;     ...
;             RT_LD(wq0, 0); RT_LD(wq1, 1);
; #pragma unroll
;             for (int t = 0; t < 30; t += 3) { RT_LD(wq2, t + 2); RT_FMA(wq0, t); RT_LD(wq0, t + 3); RT_FMA(wq1, t + 1); RT_LD(wq1, t + 4); RT_FMA(wq2, t + 2); }
	v_fma_f32 v66, v12, v0, v32
	v_mul_f32_e32 v0, v186, v169
	v_fma_f32 v64, v13, v0, v33
	v_mul_f32_e32 v0, v6, v169
	v_fma_f32 v38, v14, v0, v34
	v_mul_f32_e32 v0, v7, v169
	v_addc_co_u32_e32 v159, vcc, 0, v1, vcc
	v_fmac_f32_e32 v35, v15, v0
	v_mul_f32_e32 v0, 0x41000000, v66
	v_mul_f32_e32 v1, 0x41000000, v64
	global_store_dword v[158:159], v5, off
	v_med3_f32 v0, v0, s39, v152
	v_med3_f32 v1, v1, s39, v152
	v_cvt_pk_fp8_f32 v10, v0, v1
	ds_read_b128 v[4:7], v74
	ds_read_b128 v[26:29], v75
	v_mul_f32_e32 v8, 0x41000000, v38
	v_mul_f32_e32 v9, 0x41000000, v35
	v_med3_f32 v0, v8, s39, v152
	v_med3_f32 v1, v9, s39, v152
	v_cvt_pk_fp8_f32 v10, v0, v1 op_sel:[0,0,1]
	v_mul_f32_e32 v0, v160, v169
	s_waitcnt lgkmcnt(0)
	v_fma_f32 v36, v0, v4, v26
	v_mul_f32_e32 v0, v161, v169
	v_fma_f32 v34, v0, v5, v27
	v_mul_f32_e32 v0, v2, v169
	v_fma_f32 v32, v0, v6, v28
	v_mul_f32_e32 v0, v3, v169
	v_fmac_f32_e32 v29, v0, v7
	v_mul_f32_e32 v0, 0x41000000, v36
	v_mul_f32_e32 v1, 0x41000000, v34
	v_med3_f32 v0, v0, s39, v152
	v_med3_f32 v1, v1, s39, v152
	v_cvt_pk_fp8_f32 v16, v0, v1
	ds_read_b128 v[0:3], v76
	ds_read_b128 v[12:15], v77
	v_mul_f32_e32 v4, 0x41000000, v32
	v_mul_f32_e32 v5, 0x41000000, v29
	v_med3_f32 v4, v4, s39, v152
	v_med3_f32 v5, v5, s39, v152
	v_cvt_pk_fp8_f32 v16, v4, v5 op_sel:[0,0,1]
	v_mul_f32_e32 v4, v154, v169
	s_waitcnt lgkmcnt(0)
	v_fma_f32 v30, v4, v0, v12
	v_mul_f32_e32 v0, v155, v169
	v_fma_f32 v28, v0, v1, v13
	v_mul_f32_e32 v0, v156, v169
	v_fma_f32 v26, v0, v2, v14
	v_mul_f32_e32 v0, v31, v169
	v_fmac_f32_e32 v15, v0, v3
	v_mul_f32_e32 v0, 0x41000000, v30
	v_mul_f32_e32 v1, 0x41000000, v28
	v_med3_f32 v0, v0, s39, v152
	v_med3_f32 v1, v1, s39, v152
	v_mov_b32_e32 v4, 0
	v_cvt_pk_fp8_f32 v4, v0, v1
	v_mul_f32_e32 v2, 0x41000000, v26
	v_mul_f32_e32 v0, 0x41000000, v15
	v_med3_f32 v1, v2, s39, v152
	v_med3_f32 v0, v0, s39, v152
	v_cvt_pk_fp8_f32 v4, v1, v0 op_sel:[0,0,1]
	ds_read_b128 v[0:3], v78
	ds_read_b128 v[6:9], v79
	global_store_dword v[158:159], v10, off offset:256
	global_store_dword v[158:159], v16, off offset:512
	global_store_dword v[158:159], v4, off offset:768
	v_mul_f32_e32 v4, v22, v169
	v_mov_b32_e32 v13, 0
	s_waitcnt lgkmcnt(0)
	v_fma_f32 v24, v4, v0, v6
	v_mul_f32_e32 v0, v23, v169
	v_fma_f32 v22, v0, v1, v7
	v_mul_f32_e32 v0, v157, v169
	v_fma_f32 v20, v0, v2, v8
	v_mul_f32_e32 v0, v25, v169
	v_fmac_f32_e32 v9, v0, v3
	v_mul_f32_e32 v0, 0x41000000, v24
	v_mul_f32_e32 v1, 0x41000000, v22
	v_med3_f32 v0, v0, s39, v152
	v_med3_f32 v1, v1, s39, v152
	v_cvt_pk_fp8_f32 v13, v0, v1
	ds_read_b128 v[0:3], v80
	ds_read_b128 v[4:7], v81
	v_mul_f32_e32 v8, 0x41000000, v20
	v_mul_f32_e32 v10, 0x41000000, v9
	v_med3_f32 v8, v8, s39, v152
	v_med3_f32 v10, v10, s39, v152
	v_cvt_pk_fp8_f32 v13, v8, v10 op_sel:[0,0,1]
	v_mul_f32_e32 v8, v18, v169
	s_waitcnt lgkmcnt(0)
	v_fma_f32 v18, v8, v0, v4
	v_mul_f32_e32 v0, v19, v169
	v_fma_f32 v16, v0, v1, v5
	v_mul_f32_e32 v0, v162, v169
	v_fma_f32 v14, v0, v2, v6
	v_mul_f32_e32 v0, v21, v169
	v_fmac_f32_e32 v7, v0, v3
	v_mul_f32_e32 v0, 0x41000000, v18
	v_mul_f32_e32 v1, 0x41000000, v16
	v_med3_f32 v0, v0, s39, v152
	v_med3_f32 v1, v1, s39, v152
	v_mov_b32_e32 v19, 0
	v_cvt_pk_fp8_f32 v19, v0, v1
	ds_read_b128 v[154:157], v82
	ds_read_b128 v[2:5], v83
	v_mul_f32_e32 v6, 0x41000000, v14
	v_mul_f32_e32 v8, 0x41000000, v7
	v_med3_f32 v0, v6, s39, v152
	v_med3_f32 v1, v8, s39, v152
	v_cvt_pk_fp8_f32 v19, v0, v1 op_sel:[0,0,1]
	v_mul_f32_e32 v0, v163, v169
	s_waitcnt lgkmcnt(0)
	v_fma_f32 v12, v0, v154, v2
	v_mul_f32_e32 v0, v164, v169
	v_fma_f32 v10, v0, v155, v3
	v_mul_f32_e32 v0, v165, v169
	v_fma_f32 v8, v0, v156, v4
	v_mul_f32_e32 v0, v17, v169
	v_fmac_f32_e32 v5, v0, v157
	v_mul_f32_e32 v0, 0x41000000, v12
	v_mul_f32_e32 v1, 0x41000000, v10
	v_med3_f32 v0, v0, s39, v152
	v_med3_f32 v1, v1, s39, v152
	v_mov_b32_e32 v17, 0
	v_cvt_pk_fp8_f32 v17, v0, v1
	ds_read_b128 v[154:157], v84
	ds_read_b128 v[0:3], v85
	v_mul_f32_e32 v4, 0x41000000, v8
	v_mul_f32_e32 v6, 0x41000000, v5
	v_med3_f32 v4, v4, s39, v152
	v_med3_f32 v6, v6, s39, v152
	v_cvt_pk_fp8_f32 v17, v4, v6 op_sel:[0,0,1]
	v_mul_f32_e32 v4, v166, v169
	s_waitcnt lgkmcnt(0)
	v_fma_f32 v6, v4, v154, v0
	v_mul_f32_e32 v0, v167, v169
	v_fma_f32 v4, v0, v155, v1
	v_mul_f32_e32 v0, v168, v169
	v_mul_f32_e32 v1, v11, v169
	v_fma_f32 v0, v0, v156, v2
	v_fmac_f32_e32 v3, v1, v157
	v_mul_f32_e32 v1, 0x41000000, v6
	v_mul_f32_e32 v2, 0x41000000, v4
	v_med3_f32 v1, v1, s39, v152
	v_med3_f32 v2, v2, s39, v152
	v_mov_b32_e32 v21, 0
	v_cvt_pk_fp8_f32 v21, v1, v2
	v_mul_f32_e32 v11, 0x41000000, v0
	v_mul_f32_e32 v1, 0x41000000, v3
	v_med3_f32 v2, v11, s39, v152
	v_med3_f32 v1, v1, s39, v152
	v_cvt_pk_fp8_f32 v21, v2, v1 op_sel:[0,0,1]
	global_store_dword v[158:159], v13, off offset:1024
	global_store_dword v[158:159], v19, off offset:1280
	global_store_dword v[158:159], v17, off offset:1536
	global_store_dword v[158:159], v21, off offset:1792
	s_cmp_eq_u32 s20, 0xe000
	s_cselect_b32 s92, 0, 0x1000
	s_cselect_b32 s94, 0, 0x2000
	s_mov_b32 s93, 0
	s_mov_b32 s95, 0
	v_lshl_add_u64 v[250:251], s[46:47], 0, v[62:63]
	v_lshl_add_u64 v[252:253], v[60:61], 0, s[20:21]
	v_lshl_add_u64 v[250:251], v[250:251], 0, s[92:93]
	v_lshl_add_u64 v[252:253], v[252:253], 0, s[94:95]
	s_mov_b32 s92, 0x35800000
	s_nop 0
	v_lshl_add_u64 v[250:251], v[250:251], 0, s[92:93]
	global_load_dwordx2 v[218:219], v[250:251], off nt
	global_load_dwordx2 v[220:221], v[250:251], off offset:512 nt
	global_load_dwordx2 v[222:223], v[250:251], off offset:1024 nt
	global_load_dwordx2 v[224:225], v[250:251], off offset:1536 nt
	global_load_dwordx2 v[226:227], v[250:251], off offset:2048 nt
	global_load_dwordx2 v[228:229], v[250:251], off offset:2560 nt
	global_load_dwordx2 v[230:231], v[250:251], off offset:3072 nt
	global_load_dwordx2 v[232:233], v[250:251], off offset:3584 nt
	global_load_dwordx4 v[234:237], v[252:253], off nt
	global_load_dwordx4 v[238:241], v[252:253], off offset:1024 nt
	global_load_dwordx4 v[242:245], v[252:253], off offset:2048 nt
	global_load_dwordx4 v[246:249], v[252:253], off offset:3072 nt
	ds_read_b128 v[154:157], v86
	ds_read_b128 v[158:161], v86 offset:1024
	ds_read_b128 v[162:165], v86 offset:2048
	ds_read_b128 v[166:169], v86 offset:3072
	ds_read_b128 v[170:173], v86 offset:4096
	ds_read_b128 v[174:177], v86 offset:5120
	ds_read_b128 v[178:181], v86 offset:6144
	ds_read_b128 v[182:185], v86 offset:7168
	ds_read_b128 v[186:189], v86 offset:8192
	ds_read_b128 v[190:193], v86 offset:9216
	ds_read_b128 v[194:197], v86 offset:10240
	ds_read_b128 v[198:201], v86 offset:11264
	s_waitcnt lgkmcnt(8)
; #define RT_LD(W, t_) do { _Pragma("unroll") for (int q = 0; q < 4; ++q) W[q] = wl[((((t_)) * 4 + q) << 6) + F.lane]; } while (0)
; #define RT_FMA(W, t_) do { const float hv_ = v[(t_) >> 2][(t_) & 3]; const f32x2 hh = {hv_, hv_}; _Pragma("unroll") for (int q = 0; q < 4; ++q) { \
;                 lgp[2 * q] = __builtin_elementwise_fma(hh, (f32x2){W[q][0], W[q][1]}, lgp[2 * q]); lgp[2 * q + 1] = __builtin_elementwise_fma(hh, (f32x2){W[q][2], W[q][3]}, lgp[2 * q + 1]); } \
;                 asm volatile("" ::: "memory"); } while (0)
; DI void ph_rowpass(const Frame& F) {
;     ...
;             f32x4 wq0[4], wq1[4], wq2[4];
;     ...
;             RT_LD(wq0, 0); RT_LD(wq1, 1);
; #pragma unroll
;             for (int t = 0; t < 30; t += 3) { RT_LD(wq2, t + 2); RT_FMA(wq0, t); RT_LD(wq0, t + 3); RT_FMA(wq1, t + 1); RT_LD(wq1, t + 4); RT_FMA(wq2, t + 2); }
;             RT_FMA(wq0, 30); RT_FMA(wq1, 31);
	v_pk_fma_f32 v[204:205], v[202:203], v[154:155], 0 op_sel_hi:[0,1,0]
	v_pk_fma_f32 v[206:207], v[202:203], v[156:157], 0 op_sel_hi:[0,1,0]
	v_pk_fma_f32 v[208:209], v[202:203], v[158:159], 0 op_sel_hi:[0,1,0]
	v_pk_fma_f32 v[210:211], v[202:203], v[160:161], 0 op_sel_hi:[0,1,0]
	v_pk_fma_f32 v[212:213], v[202:203], v[162:163], 0 op_sel_hi:[0,1,0]
	v_pk_fma_f32 v[214:215], v[202:203], v[164:165], 0 op_sel_hi:[0,1,0]
	v_pk_fma_f32 v[216:217], v[202:203], v[166:167], 0 op_sel_hi:[0,1,0]
	v_pk_fma_f32 v[202:203], v[202:203], v[168:169], 0 op_sel_hi:[0,1,0]
	ds_read_b128 v[154:157], v86 offset:12288
	ds_read_b128 v[158:161], v86 offset:13312
	ds_read_b128 v[162:165], v86 offset:14336
	ds_read_b128 v[166:169], v86 offset:15360
	s_waitcnt lgkmcnt(8)
	v_pk_fma_f32 v[204:205], v[70:71], v[170:171], v[204:205] op_sel_hi:[0,1,1]
	v_pk_fma_f32 v[206:207], v[70:71], v[172:173], v[206:207] op_sel_hi:[0,1,1]
	v_pk_fma_f32 v[208:209], v[70:71], v[174:175], v[208:209] op_sel_hi:[0,1,1]
	v_pk_fma_f32 v[210:211], v[70:71], v[176:177], v[210:211] op_sel_hi:[0,1,1]
	v_pk_fma_f32 v[212:213], v[70:71], v[178:179], v[212:213] op_sel_hi:[0,1,1]
	v_pk_fma_f32 v[214:215], v[70:71], v[180:181], v[214:215] op_sel_hi:[0,1,1]
	v_pk_fma_f32 v[216:217], v[70:71], v[182:183], v[216:217] op_sel_hi:[0,1,1]
	v_pk_fma_f32 v[202:203], v[70:71], v[184:185], v[202:203] op_sel_hi:[0,1,1]
	ds_read_b128 v[170:173], v86 offset:16384
	ds_read_b128 v[174:177], v86 offset:17408
	ds_read_b128 v[178:181], v86 offset:18432
	ds_read_b128 v[182:185], v86 offset:19456
	s_waitcnt lgkmcnt(8)
	v_pk_fma_f32 v[204:205], v[68:69], v[186:187], v[204:205] op_sel_hi:[0,1,1]
	v_pk_fma_f32 v[206:207], v[68:69], v[188:189], v[206:207] op_sel_hi:[0,1,1]
	v_pk_fma_f32 v[208:209], v[68:69], v[190:191], v[208:209] op_sel_hi:[0,1,1]
	v_pk_fma_f32 v[210:211], v[68:69], v[192:193], v[210:211] op_sel_hi:[0,1,1]
	v_pk_fma_f32 v[212:213], v[68:69], v[194:195], v[212:213] op_sel_hi:[0,1,1]
	v_pk_fma_f32 v[214:215], v[68:69], v[196:197], v[214:215] op_sel_hi:[0,1,1]
	v_pk_fma_f32 v[216:217], v[68:69], v[198:199], v[216:217] op_sel_hi:[0,1,1]
	v_pk_fma_f32 v[202:203], v[68:69], v[200:201], v[202:203] op_sel_hi:[0,1,1]
	ds_read_b128 v[186:189], v86 offset:20480
	ds_read_b128 v[190:193], v86 offset:21504
	ds_read_b128 v[194:197], v86 offset:22528
	ds_read_b128 v[198:201], v86 offset:23552
	v_mov_b32_e32 v2, v39
	s_waitcnt lgkmcnt(8)
	v_pk_fma_f32 v[204:205], v[2:3], v[154:155], v[204:205] op_sel_hi:[0,1,1]
	v_pk_fma_f32 v[206:207], v[2:3], v[156:157], v[206:207] op_sel_hi:[0,1,1]
	v_pk_fma_f32 v[208:209], v[2:3], v[158:159], v[208:209] op_sel_hi:[0,1,1]
	v_pk_fma_f32 v[210:211], v[2:3], v[160:161], v[210:211] op_sel_hi:[0,1,1]
	v_pk_fma_f32 v[212:213], v[2:3], v[162:163], v[212:213] op_sel_hi:[0,1,1]
	v_pk_fma_f32 v[214:215], v[2:3], v[164:165], v[214:215] op_sel_hi:[0,1,1]
	v_pk_fma_f32 v[216:217], v[2:3], v[166:167], v[216:217] op_sel_hi:[0,1,1]
	v_pk_fma_f32 v[202:203], v[2:3], v[168:169], v[202:203] op_sel_hi:[0,1,1]
	ds_read_b128 v[154:157], v86 offset:24576
	ds_read_b128 v[158:161], v86 offset:25600
	ds_read_b128 v[162:165], v86 offset:26624
	ds_read_b128 v[166:169], v86 offset:27648
	s_waitcnt lgkmcnt(8)
	v_pk_fma_f32 v[204:205], v[66:67], v[170:171], v[204:205] op_sel_hi:[0,1,1]
	v_pk_fma_f32 v[206:207], v[66:67], v[172:173], v[206:207] op_sel_hi:[0,1,1]
	v_pk_fma_f32 v[208:209], v[66:67], v[174:175], v[208:209] op_sel_hi:[0,1,1]
	v_pk_fma_f32 v[210:211], v[66:67], v[176:177], v[210:211] op_sel_hi:[0,1,1]
	v_pk_fma_f32 v[212:213], v[66:67], v[178:179], v[212:213] op_sel_hi:[0,1,1]
	v_pk_fma_f32 v[214:215], v[66:67], v[180:181], v[214:215] op_sel_hi:[0,1,1]
	v_pk_fma_f32 v[216:217], v[66:67], v[182:183], v[216:217] op_sel_hi:[0,1,1]
	v_pk_fma_f32 v[202:203], v[66:67], v[184:185], v[202:203] op_sel_hi:[0,1,1]
	ds_read_b128 v[170:173], v86 offset:28672
	ds_read_b128 v[174:177], v86 offset:29696
	ds_read_b128 v[178:181], v86 offset:30720
	ds_read_b128 v[182:185], v86 offset:31744
	s_waitcnt lgkmcnt(8)
	v_pk_fma_f32 v[204:205], v[64:65], v[186:187], v[204:205] op_sel_hi:[0,1,1]
	v_pk_fma_f32 v[206:207], v[64:65], v[188:189], v[206:207] op_sel_hi:[0,1,1]
	v_pk_fma_f32 v[208:209], v[64:65], v[190:191], v[208:209] op_sel_hi:[0,1,1]
	v_pk_fma_f32 v[210:211], v[64:65], v[192:193], v[210:211] op_sel_hi:[0,1,1]
	v_pk_fma_f32 v[212:213], v[64:65], v[194:195], v[212:213] op_sel_hi:[0,1,1]
	v_pk_fma_f32 v[214:215], v[64:65], v[196:197], v[214:215] op_sel_hi:[0,1,1]
	v_pk_fma_f32 v[216:217], v[64:65], v[198:199], v[216:217] op_sel_hi:[0,1,1]
	v_pk_fma_f32 v[202:203], v[64:65], v[200:201], v[202:203] op_sel_hi:[0,1,1]
	ds_read_b128 v[186:189], v86 offset:32768
	ds_read_b128 v[190:193], v86 offset:33792
	ds_read_b128 v[194:197], v86 offset:34816
	ds_read_b128 v[198:201], v86 offset:35840
	s_waitcnt lgkmcnt(8)
	v_pk_fma_f32 v[204:205], v[38:39], v[154:155], v[204:205] op_sel_hi:[0,1,1]
	v_pk_fma_f32 v[206:207], v[38:39], v[156:157], v[206:207] op_sel_hi:[0,1,1]
	v_pk_fma_f32 v[208:209], v[38:39], v[158:159], v[208:209] op_sel_hi:[0,1,1]
	v_pk_fma_f32 v[210:211], v[38:39], v[160:161], v[210:211] op_sel_hi:[0,1,1]
	v_pk_fma_f32 v[212:213], v[38:39], v[162:163], v[212:213] op_sel_hi:[0,1,1]
	v_pk_fma_f32 v[214:215], v[38:39], v[164:165], v[214:215] op_sel_hi:[0,1,1]
	v_pk_fma_f32 v[216:217], v[38:39], v[166:167], v[216:217] op_sel_hi:[0,1,1]
	v_pk_fma_f32 v[38:39], v[38:39], v[168:169], v[202:203] op_sel_hi:[0,1,1]
	ds_read_b128 v[154:157], v86 offset:36864
	ds_read_b128 v[158:161], v86 offset:37888
	ds_read_b128 v[162:165], v86 offset:38912
	ds_read_b128 v[166:169], v86 offset:39936
	v_mov_b32_e32 v2, v35
	s_waitcnt lgkmcnt(8)
; #define RT_LD(W, t_) do { _Pragma("unroll") for (int q = 0; q < 4; ++q) W[q] = wl[((((t_)) * 4 + q) << 6) + F.lane]; } while (0)
; #define RT_FMA(W, t_) do { const float hv_ = v[(t_) >> 2][(t_) & 3]; const f32x2 hh = {hv_, hv_}; _Pragma("unroll") for (int q = 0; q < 4; ++q) { \
;                 lgp[2 * q] = __builtin_elementwise_fma(hh, (f32x2){W[q][0], W[q][1]}, lgp[2 * q]); lgp[2 * q + 1] = __builtin_elementwise_fma(hh, (f32x2){W[q][2], W[q][3]}, lgp[2 * q + 1]); } \
;                 asm volatile("" ::: "memory"); } while (0)
; DI void ph_rowpass(const Frame& F) {
;     ...
;             f32x4 wq0[4], wq1[4], wq2[4];
;     ...
;             RT_LD(wq0, 0); RT_LD(wq1, 1);
; #pragma unroll
;             for (int t = 0; t < 30; t += 3) { RT_LD(wq2, t + 2); RT_FMA(wq0, t); RT_LD(wq0, t + 3); RT_FMA(wq1, t + 1); RT_LD(wq1, t + 4); RT_FMA(wq2, t + 2); }
;             RT_FMA(wq0, 30); RT_FMA(wq1, 31);
	v_pk_fma_f32 v[202:203], v[2:3], v[170:171], v[204:205] op_sel_hi:[0,1,1]
	v_pk_fma_f32 v[204:205], v[2:3], v[172:173], v[206:207] op_sel_hi:[0,1,1]
	v_pk_fma_f32 v[206:207], v[2:3], v[174:175], v[208:209] op_sel_hi:[0,1,1]
	v_pk_fma_f32 v[208:209], v[2:3], v[176:177], v[210:211] op_sel_hi:[0,1,1]
	v_pk_fma_f32 v[210:211], v[2:3], v[178:179], v[212:213] op_sel_hi:[0,1,1]
	v_pk_fma_f32 v[212:213], v[2:3], v[180:181], v[214:215] op_sel_hi:[0,1,1]
	v_pk_fma_f32 v[214:215], v[2:3], v[182:183], v[216:217] op_sel_hi:[0,1,1]
	v_pk_fma_f32 v[38:39], v[2:3], v[184:185], v[38:39] op_sel_hi:[0,1,1]
	ds_read_b128 v[170:173], v86 offset:40960
	ds_read_b128 v[174:177], v86 offset:41984
	ds_read_b128 v[178:181], v86 offset:43008
	ds_read_b128 v[182:185], v86 offset:44032
	s_waitcnt lgkmcnt(8)
	v_pk_fma_f32 v[202:203], v[36:37], v[186:187], v[202:203] op_sel_hi:[0,1,1]
	v_pk_fma_f32 v[204:205], v[36:37], v[188:189], v[204:205] op_sel_hi:[0,1,1]
	v_pk_fma_f32 v[206:207], v[36:37], v[190:191], v[206:207] op_sel_hi:[0,1,1]
	v_pk_fma_f32 v[208:209], v[36:37], v[192:193], v[208:209] op_sel_hi:[0,1,1]
	v_pk_fma_f32 v[210:211], v[36:37], v[194:195], v[210:211] op_sel_hi:[0,1,1]
	v_pk_fma_f32 v[212:213], v[36:37], v[196:197], v[212:213] op_sel_hi:[0,1,1]
	v_pk_fma_f32 v[198:199], v[36:37], v[198:199], v[214:215] op_sel_hi:[0,1,1]
	v_pk_fma_f32 v[200:201], v[36:37], v[200:201], v[38:39] op_sel_hi:[0,1,1]
	ds_read_b128 v[36:39], v86 offset:45056
	ds_read_b128 v[186:189], v86 offset:46080
	ds_read_b128 v[190:193], v86 offset:47104
	ds_read_b128 v[194:197], v86 offset:48128
	s_waitcnt lgkmcnt(8)
	v_pk_fma_f32 v[202:203], v[34:35], v[154:155], v[202:203] op_sel_hi:[0,1,1]
	v_pk_fma_f32 v[204:205], v[34:35], v[156:157], v[204:205] op_sel_hi:[0,1,1]
	v_pk_fma_f32 v[206:207], v[34:35], v[158:159], v[206:207] op_sel_hi:[0,1,1]
	v_pk_fma_f32 v[208:209], v[34:35], v[160:161], v[208:209] op_sel_hi:[0,1,1]
	v_pk_fma_f32 v[210:211], v[34:35], v[162:163], v[210:211] op_sel_hi:[0,1,1]
	v_pk_fma_f32 v[212:213], v[34:35], v[164:165], v[212:213] op_sel_hi:[0,1,1]
	v_pk_fma_f32 v[198:199], v[34:35], v[166:167], v[198:199] op_sel_hi:[0,1,1]
	v_pk_fma_f32 v[34:35], v[34:35], v[168:169], v[200:201] op_sel_hi:[0,1,1]
	ds_read_b128 v[154:157], v86 offset:49152
	ds_read_b128 v[158:161], v86 offset:50176
	ds_read_b128 v[162:165], v86 offset:51200
	ds_read_b128 v[166:169], v86 offset:52224
	s_waitcnt lgkmcnt(8)
	v_pk_fma_f32 v[200:201], v[32:33], v[170:171], v[202:203] op_sel_hi:[0,1,1]
	v_pk_fma_f32 v[202:203], v[32:33], v[172:173], v[204:205] op_sel_hi:[0,1,1]
	v_pk_fma_f32 v[204:205], v[32:33], v[174:175], v[206:207] op_sel_hi:[0,1,1]
	v_pk_fma_f32 v[206:207], v[32:33], v[176:177], v[208:209] op_sel_hi:[0,1,1]
	v_pk_fma_f32 v[208:209], v[32:33], v[178:179], v[210:211] op_sel_hi:[0,1,1]
	v_pk_fma_f32 v[210:211], v[32:33], v[180:181], v[212:213] op_sel_hi:[0,1,1]
	v_pk_fma_f32 v[182:183], v[32:33], v[182:183], v[198:199] op_sel_hi:[0,1,1]
	v_pk_fma_f32 v[184:185], v[32:33], v[184:185], v[34:35] op_sel_hi:[0,1,1]
	ds_read_b128 v[32:35], v86 offset:53248
	ds_read_b128 v[170:173], v86 offset:54272
	ds_read_b128 v[174:177], v86 offset:55296
	ds_read_b128 v[178:181], v86 offset:56320
	v_mov_b32_e32 v2, v29
	s_waitcnt lgkmcnt(8)
	v_pk_fma_f32 v[198:199], v[2:3], v[36:37], v[200:201] op_sel_hi:[0,1,1]
	v_pk_fma_f32 v[200:201], v[2:3], v[38:39], v[202:203] op_sel_hi:[0,1,1]
	v_pk_fma_f32 v[202:203], v[2:3], v[186:187], v[204:205] op_sel_hi:[0,1,1]
	v_pk_fma_f32 v[204:205], v[2:3], v[188:189], v[206:207] op_sel_hi:[0,1,1]
	v_pk_fma_f32 v[206:207], v[2:3], v[190:191], v[208:209] op_sel_hi:[0,1,1]
	v_pk_fma_f32 v[208:209], v[2:3], v[192:193], v[210:211] op_sel_hi:[0,1,1]
	v_pk_fma_f32 v[194:195], v[2:3], v[194:195], v[182:183] op_sel_hi:[0,1,1]
	v_pk_fma_f32 v[196:197], v[2:3], v[196:197], v[184:185] op_sel_hi:[0,1,1]
	ds_read_b128 v[36:39], v86 offset:57344
	ds_read_b128 v[182:185], v86 offset:58368
	ds_read_b128 v[186:189], v86 offset:59392
	ds_read_b128 v[190:193], v86 offset:60416
	s_waitcnt lgkmcnt(8)
	v_pk_fma_f32 v[198:199], v[30:31], v[154:155], v[198:199] op_sel_hi:[0,1,1]
	v_pk_fma_f32 v[200:201], v[30:31], v[156:157], v[200:201] op_sel_hi:[0,1,1]
	v_pk_fma_f32 v[202:203], v[30:31], v[158:159], v[202:203] op_sel_hi:[0,1,1]
	v_pk_fma_f32 v[204:205], v[30:31], v[160:161], v[204:205] op_sel_hi:[0,1,1]
	v_pk_fma_f32 v[206:207], v[30:31], v[162:163], v[206:207] op_sel_hi:[0,1,1]
	v_pk_fma_f32 v[208:209], v[30:31], v[164:165], v[208:209] op_sel_hi:[0,1,1]
	v_pk_fma_f32 v[194:195], v[30:31], v[166:167], v[194:195] op_sel_hi:[0,1,1]
	v_pk_fma_f32 v[30:31], v[30:31], v[168:169], v[196:197] op_sel_hi:[0,1,1]
	ds_read_b128 v[154:157], v86 offset:61440
	ds_read_b128 v[158:161], v86 offset:62464
	ds_read_b128 v[162:165], v86 offset:63488
	ds_read_b128 v[166:169], v86 offset:64512
	s_waitcnt lgkmcnt(8)
	v_pk_fma_f32 v[196:197], v[28:29], v[32:33], v[198:199] op_sel_hi:[0,1,1]
	v_pk_fma_f32 v[198:199], v[28:29], v[34:35], v[200:201] op_sel_hi:[0,1,1]
	v_pk_fma_f32 v[200:201], v[28:29], v[170:171], v[202:203] op_sel_hi:[0,1,1]
	v_pk_fma_f32 v[202:203], v[28:29], v[172:173], v[204:205] op_sel_hi:[0,1,1]
	v_pk_fma_f32 v[204:205], v[28:29], v[174:175], v[206:207] op_sel_hi:[0,1,1]
	v_pk_fma_f32 v[206:207], v[28:29], v[176:177], v[208:209] op_sel_hi:[0,1,1]
	v_pk_fma_f32 v[178:179], v[28:29], v[178:179], v[194:195] op_sel_hi:[0,1,1]
	v_pk_fma_f32 v[180:181], v[28:29], v[180:181], v[30:31] op_sel_hi:[0,1,1]
	ds_read_b128 v[28:31], v87
	ds_read_b128 v[32:35], v88
	ds_read_b128 v[170:173], v89
	ds_read_b128 v[174:177], v90
	s_waitcnt lgkmcnt(8)
; #define RT_LD(W, t_) do { _Pragma("unroll") for (int q = 0; q < 4; ++q) W[q] = wl[((((t_)) * 4 + q) << 6) + F.lane]; } while (0)
; #define RT_FMA(W, t_) do { const float hv_ = v[(t_) >> 2][(t_) & 3]; const f32x2 hh = {hv_, hv_}; _Pragma("unroll") for (int q = 0; q < 4; ++q) { \
;                 lgp[2 * q] = __builtin_elementwise_fma(hh, (f32x2){W[q][0], W[q][1]}, lgp[2 * q]); lgp[2 * q + 1] = __builtin_elementwise_fma(hh, (f32x2){W[q][2], W[q][3]}, lgp[2 * q + 1]); } \
;                 asm volatile("" ::: "memory"); } while (0)
; DI void ph_rowpass(const Frame& F) {
;     ...
;             f32x4 wq0[4], wq1[4], wq2[4];
;     ...
;             RT_LD(wq0, 0); RT_LD(wq1, 1);
; #pragma unroll
;             for (int t = 0; t < 30; t += 3) { RT_LD(wq2, t + 2); RT_FMA(wq0, t); RT_LD(wq0, t + 3); RT_FMA(wq1, t + 1); RT_LD(wq1, t + 4); RT_FMA(wq2, t + 2); }
;             RT_FMA(wq0, 30); RT_FMA(wq1, 31);
	v_pk_fma_f32 v[194:195], v[26:27], v[36:37], v[196:197] op_sel_hi:[0,1,1]
	v_pk_fma_f32 v[196:197], v[26:27], v[38:39], v[198:199] op_sel_hi:[0,1,1]
	v_pk_fma_f32 v[198:199], v[26:27], v[182:183], v[200:201] op_sel_hi:[0,1,1]
	v_pk_fma_f32 v[200:201], v[26:27], v[184:185], v[202:203] op_sel_hi:[0,1,1]
	v_pk_fma_f32 v[202:203], v[26:27], v[186:187], v[204:205] op_sel_hi:[0,1,1]
	v_pk_fma_f32 v[204:205], v[26:27], v[188:189], v[206:207] op_sel_hi:[0,1,1]
	v_pk_fma_f32 v[190:191], v[26:27], v[190:191], v[178:179] op_sel_hi:[0,1,1]
	v_pk_fma_f32 v[26:27], v[26:27], v[192:193], v[180:181] op_sel_hi:[0,1,1]
	ds_read_b128 v[36:39], v91
	ds_read_b128 v[178:181], v92
	ds_read_b128 v[182:185], v93
	ds_read_b128 v[186:189], v94
	v_mov_b32_e32 v2, v15
	s_waitcnt lgkmcnt(8)
	v_pk_fma_f32 v[192:193], v[2:3], v[154:155], v[194:195] op_sel_hi:[0,1,1]
	v_pk_fma_f32 v[194:195], v[2:3], v[156:157], v[196:197] op_sel_hi:[0,1,1]
	v_pk_fma_f32 v[196:197], v[2:3], v[158:159], v[198:199] op_sel_hi:[0,1,1]
	v_pk_fma_f32 v[198:199], v[2:3], v[160:161], v[200:201] op_sel_hi:[0,1,1]
	v_pk_fma_f32 v[200:201], v[2:3], v[162:163], v[202:203] op_sel_hi:[0,1,1]
	v_pk_fma_f32 v[202:203], v[2:3], v[164:165], v[204:205] op_sel_hi:[0,1,1]
	v_pk_fma_f32 v[190:191], v[2:3], v[166:167], v[190:191] op_sel_hi:[0,1,1]
	v_pk_fma_f32 v[26:27], v[2:3], v[168:169], v[26:27] op_sel_hi:[0,1,1]
	ds_read_b128 v[154:157], v95
	ds_read_b128 v[158:161], v96
	ds_read_b128 v[162:165], v97
	ds_read_b128 v[166:169], v98
	s_waitcnt lgkmcnt(8)
	v_pk_fma_f32 v[192:193], v[24:25], v[28:29], v[192:193] op_sel_hi:[0,1,1]
	v_pk_fma_f32 v[194:195], v[24:25], v[30:31], v[194:195] op_sel_hi:[0,1,1]
	v_pk_fma_f32 v[196:197], v[24:25], v[32:33], v[196:197] op_sel_hi:[0,1,1]
	v_pk_fma_f32 v[198:199], v[24:25], v[34:35], v[198:199] op_sel_hi:[0,1,1]
	v_pk_fma_f32 v[200:201], v[24:25], v[170:171], v[200:201] op_sel_hi:[0,1,1]
	v_pk_fma_f32 v[202:203], v[24:25], v[172:173], v[202:203] op_sel_hi:[0,1,1]
	v_pk_fma_f32 v[174:175], v[24:25], v[174:175], v[190:191] op_sel_hi:[0,1,1]
	v_pk_fma_f32 v[176:177], v[24:25], v[176:177], v[26:27] op_sel_hi:[0,1,1]
	ds_read_b128 v[24:27], v99
	ds_read_b128 v[28:31], v100
	ds_read_b128 v[32:35], v101
	ds_read_b128 v[170:173], v102
	s_waitcnt lgkmcnt(8)
	v_pk_fma_f32 v[190:191], v[22:23], v[36:37], v[192:193] op_sel_hi:[0,1,1]
	v_pk_fma_f32 v[192:193], v[22:23], v[38:39], v[194:195] op_sel_hi:[0,1,1]
	v_pk_fma_f32 v[194:195], v[22:23], v[178:179], v[196:197] op_sel_hi:[0,1,1]
	v_pk_fma_f32 v[196:197], v[22:23], v[180:181], v[198:199] op_sel_hi:[0,1,1]
	v_pk_fma_f32 v[198:199], v[22:23], v[182:183], v[200:201] op_sel_hi:[0,1,1]
	v_pk_fma_f32 v[200:201], v[22:23], v[184:185], v[202:203] op_sel_hi:[0,1,1]
	v_pk_fma_f32 v[186:187], v[22:23], v[186:187], v[174:175] op_sel_hi:[0,1,1]
	v_pk_fma_f32 v[22:23], v[22:23], v[188:189], v[176:177] op_sel_hi:[0,1,1]
	ds_read_b128 v[36:39], v103
	ds_read_b128 v[174:177], v104
	ds_read_b128 v[178:181], v105
	ds_read_b128 v[182:185], v106
	s_waitcnt lgkmcnt(8)
	v_pk_fma_f32 v[188:189], v[20:21], v[154:155], v[190:191] op_sel_hi:[0,1,1]
	v_pk_fma_f32 v[190:191], v[20:21], v[156:157], v[192:193] op_sel_hi:[0,1,1]
	v_pk_fma_f32 v[192:193], v[20:21], v[158:159], v[194:195] op_sel_hi:[0,1,1]
	v_pk_fma_f32 v[194:195], v[20:21], v[160:161], v[196:197] op_sel_hi:[0,1,1]
	v_pk_fma_f32 v[196:197], v[20:21], v[162:163], v[198:199] op_sel_hi:[0,1,1]
	v_pk_fma_f32 v[198:199], v[20:21], v[164:165], v[200:201] op_sel_hi:[0,1,1]
	v_pk_fma_f32 v[166:167], v[20:21], v[166:167], v[186:187] op_sel_hi:[0,1,1]
	v_pk_fma_f32 v[168:169], v[20:21], v[168:169], v[22:23] op_sel_hi:[0,1,1]
	ds_read_b128 v[20:23], v107
	ds_read_b128 v[154:157], v108
	ds_read_b128 v[158:161], v109
	ds_read_b128 v[162:165], v110
	v_mov_b32_e32 v2, v9
	s_waitcnt lgkmcnt(8)
	v_pk_fma_f32 v[186:187], v[2:3], v[24:25], v[188:189] op_sel_hi:[0,1,1]
	v_pk_fma_f32 v[188:189], v[2:3], v[26:27], v[190:191] op_sel_hi:[0,1,1]
	v_pk_fma_f32 v[190:191], v[2:3], v[28:29], v[192:193] op_sel_hi:[0,1,1]
	v_pk_fma_f32 v[192:193], v[2:3], v[30:31], v[194:195] op_sel_hi:[0,1,1]
	v_pk_fma_f32 v[194:195], v[2:3], v[32:33], v[196:197] op_sel_hi:[0,1,1]
	v_pk_fma_f32 v[196:197], v[2:3], v[34:35], v[198:199] op_sel_hi:[0,1,1]
	v_pk_fma_f32 v[170:171], v[2:3], v[170:171], v[166:167] op_sel_hi:[0,1,1]
	v_pk_fma_f32 v[172:173], v[2:3], v[172:173], v[168:169] op_sel_hi:[0,1,1]
	ds_read_b128 v[24:27], v111
	ds_read_b128 v[28:31], v112
	ds_read_b128 v[32:35], v113
	ds_read_b128 v[166:169], v114
	s_waitcnt lgkmcnt(8)
	v_pk_fma_f32 v[186:187], v[18:19], v[36:37], v[186:187] op_sel_hi:[0,1,1]
	v_pk_fma_f32 v[188:189], v[18:19], v[38:39], v[188:189] op_sel_hi:[0,1,1]
	v_pk_fma_f32 v[190:191], v[18:19], v[174:175], v[190:191] op_sel_hi:[0,1,1]
	v_pk_fma_f32 v[192:193], v[18:19], v[176:177], v[192:193] op_sel_hi:[0,1,1]
	v_pk_fma_f32 v[194:195], v[18:19], v[178:179], v[194:195] op_sel_hi:[0,1,1]
	v_pk_fma_f32 v[196:197], v[18:19], v[180:181], v[196:197] op_sel_hi:[0,1,1]
	v_pk_fma_f32 v[182:183], v[18:19], v[182:183], v[170:171] op_sel_hi:[0,1,1]
	v_pk_fma_f32 v[18:19], v[18:19], v[184:185], v[172:173] op_sel_hi:[0,1,1]
	ds_read_b128 v[36:39], v115
	ds_read_b128 v[170:173], v116
	ds_read_b128 v[174:177], v117
	ds_read_b128 v[178:181], v118
	s_waitcnt lgkmcnt(8)
; #define RT_LD(W, t_) do { _Pragma("unroll") for (int q = 0; q < 4; ++q) W[q] = wl[((((t_)) * 4 + q) << 6) + F.lane]; } while (0)
; #define RT_FMA(W, t_) do { const float hv_ = v[(t_) >> 2][(t_) & 3]; const f32x2 hh = {hv_, hv_}; _Pragma("unroll") for (int q = 0; q < 4; ++q) { \
;                 lgp[2 * q] = __builtin_elementwise_fma(hh, (f32x2){W[q][0], W[q][1]}, lgp[2 * q]); lgp[2 * q + 1] = __builtin_elementwise_fma(hh, (f32x2){W[q][2], W[q][3]}, lgp[2 * q + 1]); } \
;                 asm volatile("" ::: "memory"); } while (0)
; DI void ph_rowpass(const Frame& F) {
;     ...
;             f32x4 wq0[4], wq1[4], wq2[4];
;     ...
;             RT_LD(wq0, 0); RT_LD(wq1, 1);
; #pragma unroll
;             for (int t = 0; t < 30; t += 3) { RT_LD(wq2, t + 2); RT_FMA(wq0, t); RT_LD(wq0, t + 3); RT_FMA(wq1, t + 1); RT_LD(wq1, t + 4); RT_FMA(wq2, t + 2); }
;             RT_FMA(wq0, 30); RT_FMA(wq1, 31);
	v_pk_fma_f32 v[184:185], v[16:17], v[20:21], v[186:187] op_sel_hi:[0,1,1]
	v_pk_fma_f32 v[186:187], v[16:17], v[22:23], v[188:189] op_sel_hi:[0,1,1]
	v_pk_fma_f32 v[188:189], v[16:17], v[154:155], v[190:191] op_sel_hi:[0,1,1]
	v_pk_fma_f32 v[190:191], v[16:17], v[156:157], v[192:193] op_sel_hi:[0,1,1]
	v_pk_fma_f32 v[192:193], v[16:17], v[158:159], v[194:195] op_sel_hi:[0,1,1]
	v_pk_fma_f32 v[194:195], v[16:17], v[160:161], v[196:197] op_sel_hi:[0,1,1]
	v_pk_fma_f32 v[162:163], v[16:17], v[162:163], v[182:183] op_sel_hi:[0,1,1]
	v_pk_fma_f32 v[164:165], v[16:17], v[164:165], v[18:19] op_sel_hi:[0,1,1]
	ds_read_b128 v[16:19], v119
	ds_read_b128 v[20:23], v120
	ds_read_b128 v[154:157], v121
	ds_read_b128 v[158:161], v122
	s_waitcnt lgkmcnt(8)
	v_pk_fma_f32 v[182:183], v[14:15], v[24:25], v[184:185] op_sel_hi:[0,1,1]
	v_pk_fma_f32 v[184:185], v[14:15], v[26:27], v[186:187] op_sel_hi:[0,1,1]
	v_pk_fma_f32 v[186:187], v[14:15], v[28:29], v[188:189] op_sel_hi:[0,1,1]
	v_pk_fma_f32 v[188:189], v[14:15], v[30:31], v[190:191] op_sel_hi:[0,1,1]
	v_pk_fma_f32 v[190:191], v[14:15], v[32:33], v[192:193] op_sel_hi:[0,1,1]
	v_pk_fma_f32 v[192:193], v[14:15], v[34:35], v[194:195] op_sel_hi:[0,1,1]
	v_pk_fma_f32 v[166:167], v[14:15], v[166:167], v[162:163] op_sel_hi:[0,1,1]
	v_pk_fma_f32 v[14:15], v[14:15], v[168:169], v[164:165] op_sel_hi:[0,1,1]
	ds_read_b128 v[24:27], v123
	ds_read_b128 v[28:31], v124
	ds_read_b128 v[32:35], v125
	ds_read_b128 v[162:165], v126
	v_mov_b32_e32 v2, v7
	s_waitcnt lgkmcnt(8)
	v_pk_fma_f32 v[182:183], v[2:3], v[36:37], v[182:183] op_sel_hi:[0,1,1]
	v_pk_fma_f32 v[184:185], v[2:3], v[38:39], v[184:185] op_sel_hi:[0,1,1]
	v_pk_fma_f32 v[186:187], v[2:3], v[170:171], v[186:187] op_sel_hi:[0,1,1]
	v_pk_fma_f32 v[188:189], v[2:3], v[172:173], v[188:189] op_sel_hi:[0,1,1]
	v_pk_fma_f32 v[190:191], v[2:3], v[174:175], v[190:191] op_sel_hi:[0,1,1]
	v_pk_fma_f32 v[192:193], v[2:3], v[176:177], v[192:193] op_sel_hi:[0,1,1]
	v_pk_fma_f32 v[178:179], v[2:3], v[178:179], v[166:167] op_sel_hi:[0,1,1]
	v_pk_fma_f32 v[14:15], v[2:3], v[180:181], v[14:15] op_sel_hi:[0,1,1]
	ds_read_b128 v[36:39], v127
	ds_read_b128 v[166:169], v128
	ds_read_b128 v[170:173], v129
	ds_read_b128 v[174:177], v130
	s_waitcnt lgkmcnt(8)
	v_pk_fma_f32 v[180:181], v[12:13], v[16:17], v[182:183] op_sel_hi:[0,1,1]
	v_pk_fma_f32 v[182:183], v[12:13], v[18:19], v[184:185] op_sel_hi:[0,1,1]
	v_pk_fma_f32 v[184:185], v[12:13], v[20:21], v[186:187] op_sel_hi:[0,1,1]
	v_pk_fma_f32 v[186:187], v[12:13], v[22:23], v[188:189] op_sel_hi:[0,1,1]
	v_pk_fma_f32 v[188:189], v[12:13], v[154:155], v[190:191] op_sel_hi:[0,1,1]
	v_pk_fma_f32 v[190:191], v[12:13], v[156:157], v[192:193] op_sel_hi:[0,1,1]
	v_pk_fma_f32 v[158:159], v[12:13], v[158:159], v[178:179] op_sel_hi:[0,1,1]
	v_pk_fma_f32 v[160:161], v[12:13], v[160:161], v[14:15] op_sel_hi:[0,1,1]
	ds_read_b128 v[12:15], v131
	ds_read_b128 v[16:19], v132
	ds_read_b128 v[20:23], v133
	ds_read_b128 v[154:157], v134
	s_waitcnt lgkmcnt(8)
	v_pk_fma_f32 v[178:179], v[10:11], v[24:25], v[180:181] op_sel_hi:[0,1,1]
	v_pk_fma_f32 v[180:181], v[10:11], v[26:27], v[182:183] op_sel_hi:[0,1,1]
	v_pk_fma_f32 v[182:183], v[10:11], v[28:29], v[184:185] op_sel_hi:[0,1,1]
	v_pk_fma_f32 v[184:185], v[10:11], v[30:31], v[186:187] op_sel_hi:[0,1,1]
	v_pk_fma_f32 v[186:187], v[10:11], v[32:33], v[188:189] op_sel_hi:[0,1,1]
	v_pk_fma_f32 v[188:189], v[10:11], v[34:35], v[190:191] op_sel_hi:[0,1,1]
	v_pk_fma_f32 v[162:163], v[10:11], v[162:163], v[158:159] op_sel_hi:[0,1,1]
	v_pk_fma_f32 v[10:11], v[10:11], v[164:165], v[160:161] op_sel_hi:[0,1,1]
	ds_read_b128 v[24:27], v135
	ds_read_b128 v[28:31], v136
	ds_read_b128 v[32:35], v137
	ds_read_b128 v[158:161], v138
	s_waitcnt lgkmcnt(8)
	v_pk_fma_f32 v[178:179], v[8:9], v[36:37], v[178:179] op_sel_hi:[0,1,1]
	v_pk_fma_f32 v[180:181], v[8:9], v[38:39], v[180:181] op_sel_hi:[0,1,1]
	v_pk_fma_f32 v[182:183], v[8:9], v[166:167], v[182:183] op_sel_hi:[0,1,1]
	v_pk_fma_f32 v[184:185], v[8:9], v[168:169], v[184:185] op_sel_hi:[0,1,1]
	v_pk_fma_f32 v[170:171], v[8:9], v[170:171], v[186:187] op_sel_hi:[0,1,1]
	v_pk_fma_f32 v[172:173], v[8:9], v[172:173], v[188:189] op_sel_hi:[0,1,1]
	v_pk_fma_f32 v[174:175], v[8:9], v[174:175], v[162:163] op_sel_hi:[0,1,1]
	v_pk_fma_f32 v[176:177], v[8:9], v[176:177], v[10:11] op_sel_hi:[0,1,1]
	ds_read_b128 v[8:11], v139
	ds_read_b128 v[36:39], v140
	ds_read_b128 v[162:165], v141
	ds_read_b128 v[166:169], v142
	v_mov_b32_e32 v2, v5
	s_waitcnt lgkmcnt(8)
	v_pk_fma_f32 v[178:179], v[2:3], v[12:13], v[178:179] op_sel_hi:[0,1,1]
	v_pk_fma_f32 v[180:181], v[2:3], v[14:15], v[180:181] op_sel_hi:[0,1,1]
	v_pk_fma_f32 v[182:183], v[2:3], v[16:17], v[182:183] op_sel_hi:[0,1,1]
	v_pk_fma_f32 v[184:185], v[2:3], v[18:19], v[184:185] op_sel_hi:[0,1,1]
	v_pk_fma_f32 v[170:171], v[2:3], v[20:21], v[170:171] op_sel_hi:[0,1,1]
	v_pk_fma_f32 v[172:173], v[2:3], v[22:23], v[172:173] op_sel_hi:[0,1,1]
	v_pk_fma_f32 v[174:175], v[2:3], v[154:155], v[174:175] op_sel_hi:[0,1,1]
	v_pk_fma_f32 v[176:177], v[2:3], v[156:157], v[176:177] op_sel_hi:[0,1,1]
	ds_read_b128 v[12:15], v143
	ds_read_b128 v[16:19], v144
	ds_read_b128 v[20:23], v145
	ds_read_b128 v[154:157], v146
	s_waitcnt lgkmcnt(8)
	v_pk_fma_f32 v[178:179], v[6:7], v[24:25], v[178:179] op_sel_hi:[0,1,1]
	v_pk_fma_f32 v[180:181], v[6:7], v[26:27], v[180:181] op_sel_hi:[0,1,1]
	v_pk_fma_f32 v[182:183], v[6:7], v[28:29], v[182:183] op_sel_hi:[0,1,1]
	v_pk_fma_f32 v[184:185], v[6:7], v[30:31], v[184:185] op_sel_hi:[0,1,1]
	v_pk_fma_f32 v[170:171], v[6:7], v[32:33], v[170:171] op_sel_hi:[0,1,1]
	v_pk_fma_f32 v[172:173], v[6:7], v[34:35], v[172:173] op_sel_hi:[0,1,1]
	v_pk_fma_f32 v[174:175], v[6:7], v[158:159], v[174:175] op_sel_hi:[0,1,1]
	v_pk_fma_f32 v[6:7], v[6:7], v[160:161], v[176:177] op_sel_hi:[0,1,1]
	ds_read_b128 v[24:27], v147
	ds_read_b128 v[28:31], v148
	ds_read_b128 v[32:35], v149
	ds_read_b128 v[158:161], v150
	s_waitcnt lgkmcnt(8)
; DI float swz16_f(float v) { return __builtin_bit_cast(float, __builtin_amdgcn_ds_swizzle(__builtin_bit_cast(int, v), 0x401F)); }
; #define RT_LD(W, t_) do { _Pragma("unroll") for (int q = 0; q < 4; ++q) W[q] = wl[((((t_)) * 4 + q) << 6) + F.lane]; } while (0)
; DI float expert_totals16(const f32x2 (&p)[8], int lane) {
;     float y[8];
; #pragma unroll
;     for (int i = 0; i < 8; ++i) { const float a = p[i >> 1][i & 1], b = p[(i + 8) >> 1][i & 1];
;         auto r = __builtin_amdgcn_permlane32_swap(__float_as_uint(a), __float_as_uint(b), false, false); y[i] = __uint_as_float(r[0]) + __uint_as_float(r[1]); }
;     const bool b4 = (lane & 16) != 0, b3 = (lane & 8) != 0, b2 = (lane & 4) != 0;
;     float z[4];
; #pragma unroll
;     for (int i = 0; i < 4; ++i) { const float send = b4 ? y[i] : y[i + 4], keep = b4 ? y[i + 4] : y[i]; z[i] = keep + swz16_f(send); }
;     float w[2];
; #pragma unroll
;     for (int i = 0; i < 2; ++i) { const float send = b3 ? z[i] : z[i + 2], keep = b3 ? z[i + 2] : z[i]; w[i] = keep + dpp_f(send, 0x128); }
;     float v; { const float send = b2 ? w[0] : w[1], keep = b2 ? w[1] : w[0]; v = keep + dpp_f(send, 0x141); }
;     v += dpp_f(v, 0xB1); v += dpp_f(v, 0x4E);
;     return v;
; }
; DI float experts_max(float v) { v = fmaxf(v, dpp_f(v, 0x141)); v = fmaxf(v, dpp_f(v, 0x140)); v = fmaxf(v, swz16_f(v));
;     auto r = __builtin_amdgcn_permlane32_swap(__float_as_uint(v), __float_as_uint(v), false, false); return fmaxf(__uint_as_float(r[0]), __uint_as_float(r[1])); }
; DI float experts_sum(float v) { v += dpp_f(v, 0x141); v += dpp_f(v, 0x140); v += swz16_f(v);
;     auto r = __builtin_amdgcn_permlane32_swap(__float_as_uint(v), __float_as_uint(v), false, false); return __uint_as_float(r[0]) + __uint_as_float(r[1]); }
; DI void ph_rowpass(const Frame& F) {
;     ...
;             for (int t = 0; t < 30; t += 3) { RT_LD(wq2, t + 2); RT_FMA(wq0, t); RT_LD(wq0, t + 3); RT_FMA(wq1, t + 1); RT_LD(wq1, t + 4); RT_FMA(wq2, t + 2); }
;             RT_FMA(wq0, 30); RT_FMA(wq1, 31);
;     ...
;         }
;         {
;             const float tot = expert_totals16(lgp, F.lane);
;             const float pe = __expf(tot - experts_max(tot));
;             const float prob = pe * (1.f / experts_sum(pe));
;             if ((F.lane & 3) == 0) AFF[((size_t)b * NE + (F.lane >> 2)) * S + s] = prob;
	v_pk_fma_f32 v[8:9], v[4:5], v[8:9], v[178:179] op_sel_hi:[0,1,1]
	v_pk_fma_f32 v[10:11], v[4:5], v[10:11], v[180:181] op_sel_hi:[0,1,1]
	v_pk_fma_f32 v[36:37], v[4:5], v[36:37], v[182:183] op_sel_hi:[0,1,1]
	v_pk_fma_f32 v[38:39], v[4:5], v[38:39], v[184:185] op_sel_hi:[0,1,1]
	v_pk_fma_f32 v[162:163], v[4:5], v[162:163], v[170:171] op_sel_hi:[0,1,1]
	v_pk_fma_f32 v[164:165], v[4:5], v[164:165], v[172:173] op_sel_hi:[0,1,1]
	v_pk_fma_f32 v[166:167], v[4:5], v[166:167], v[174:175] op_sel_hi:[0,1,1]
	v_pk_fma_f32 v[4:5], v[4:5], v[168:169], v[6:7] op_sel_hi:[0,1,1]
	s_waitcnt lgkmcnt(7)
	v_pk_fma_f32 v[6:7], v[0:1], v[12:13], v[8:9] op_sel_hi:[0,1,1]
	v_pk_fma_f32 v[8:9], v[0:1], v[14:15], v[10:11] op_sel_hi:[0,1,1]
	s_waitcnt lgkmcnt(6)
	v_pk_fma_f32 v[10:11], v[0:1], v[16:17], v[36:37] op_sel_hi:[0,1,1]
	v_pk_fma_f32 v[12:13], v[0:1], v[18:19], v[38:39] op_sel_hi:[0,1,1]
	s_waitcnt lgkmcnt(5)
	v_pk_fma_f32 v[14:15], v[0:1], v[20:21], v[162:163] op_sel_hi:[0,1,1]
	v_pk_fma_f32 v[16:17], v[0:1], v[22:23], v[164:165] op_sel_hi:[0,1,1]
	s_waitcnt lgkmcnt(4)
	v_pk_fma_f32 v[18:19], v[0:1], v[154:155], v[166:167] op_sel_hi:[0,1,1]
	v_mov_b32_e32 v2, v3
	v_pk_fma_f32 v[0:1], v[0:1], v[156:157], v[4:5] op_sel_hi:[0,1,1]
	s_waitcnt lgkmcnt(3)
	v_pk_fma_f32 v[4:5], v[2:3], v[24:25], v[6:7] op_sel_hi:[0,1,1]
	v_pk_fma_f32 v[6:7], v[2:3], v[26:27], v[8:9] op_sel_hi:[0,1,1]
	s_waitcnt lgkmcnt(2)
	v_pk_fma_f32 v[8:9], v[2:3], v[28:29], v[10:11] op_sel_hi:[0,1,1]
	v_pk_fma_f32 v[10:11], v[2:3], v[30:31], v[12:13] op_sel_hi:[0,1,1]
	s_waitcnt lgkmcnt(1)
	v_pk_fma_f32 v[12:13], v[2:3], v[32:33], v[14:15] op_sel_hi:[0,1,1]
	v_pk_fma_f32 v[14:15], v[2:3], v[34:35], v[16:17] op_sel_hi:[0,1,1]
	s_waitcnt lgkmcnt(0)
	v_pk_fma_f32 v[16:17], v[2:3], v[158:159], v[18:19] op_sel_hi:[0,1,1]
	v_permlane32_swap_b32_e32 v4, v12
	v_permlane32_swap_b32_e32 v6, v14
	v_permlane32_swap_b32_e32 v8, v16
	v_pk_fma_f32 v[0:1], v[2:3], v[160:161], v[0:1] op_sel_hi:[0,1,1]
	v_add_f32_e32 v2, v4, v12
	v_add_f32_e32 v4, v6, v14
	v_add_f32_e32 v6, v8, v16
	v_cndmask_b32_e64 v8, v2, v6, s[2:3]
	ds_swizzle_b32 v8, v8 offset:swizzle(SWAP,16)
	v_permlane32_swap_b32_e32 v5, v13
	v_permlane32_swap_b32_e32 v7, v15
	v_permlane32_swap_b32_e32 v9, v17
	v_permlane32_swap_b32_e32 v10, v0
	v_permlane32_swap_b32_e32 v11, v1
	v_add_f32_e32 v3, v5, v13
	v_add_f32_e32 v5, v7, v15
	v_add_f32_e32 v7, v9, v17
	v_add_f32_e32 v0, v10, v0
	v_add_f32_e32 v1, v11, v1
	v_cndmask_b32_e64 v2, v6, v2, s[2:3]
	s_waitcnt lgkmcnt(0)
	v_add_f32_e32 v2, v2, v8
	v_cndmask_b32_e64 v6, v3, v7, s[2:3]
	v_cndmask_b32_e64 v3, v7, v3, s[2:3]
	v_cndmask_b32_e64 v7, v4, v0, s[2:3]
	v_cndmask_b32_e64 v8, v5, v1, s[2:3]
	ds_swizzle_b32 v6, v6 offset:swizzle(SWAP,16)
	ds_swizzle_b32 v7, v7 offset:swizzle(SWAP,16)
	ds_swizzle_b32 v8, v8 offset:swizzle(SWAP,16)
	v_cndmask_b32_e64 v0, v0, v4, s[2:3]
	v_cndmask_b32_e64 v1, v1, v5, s[2:3]
	s_waitcnt lgkmcnt(2)
	v_add_f32_e32 v3, v3, v6
	s_waitcnt lgkmcnt(1)
	v_add_f32_e32 v0, v0, v7
	s_waitcnt lgkmcnt(0)
	v_add_f32_e32 v1, v1, v8
	v_cndmask_b32_e64 v4, v2, v0, s[4:5]
	v_cndmask_b32_e64 v0, v0, v2, s[4:5]
	v_cndmask_b32_e64 v2, v3, v1, s[4:5]
	v_cndmask_b32_e64 v1, v1, v3, s[4:5]
	v_add_f32_dpp v0, v4, v0 row_ror:8 row_mask:0xf bank_mask:0xf bound_ctrl:1
	s_nop 0
	v_add_f32_dpp v1, v2, v1 row_ror:8 row_mask:0xf bank_mask:0xf bound_ctrl:1
	v_cndmask_b32_e64 v2, v0, v1, s[6:7]
	v_cndmask_b32_e64 v0, v1, v0, s[6:7]
	s_nop 1
	v_add_f32_dpp v0, v2, v0 row_half_mirror row_mask:0xf bank_mask:0xf bound_ctrl:1
	s_nop 1
	v_add_f32_dpp v0, v0, v0 quad_perm:[1,0,3,2] row_mask:0xf bank_mask:0xf bound_ctrl:1
	s_nop 1
	v_add_f32_dpp v0, v0, v0 quad_perm:[2,3,0,1] row_mask:0xf bank_mask:0xf bound_ctrl:1
	s_nop 1
	v_mov_b32_dpp v1, v0 row_half_mirror row_mask:0xf bank_mask:0xf bound_ctrl:1
	v_max_f32_e32 v1, v1, v1
	v_max_f32_e32 v1, v0, v1
	s_nop 1
	v_mov_b32_dpp v2, v1 row_mirror row_mask:0xf bank_mask:0xf bound_ctrl:1
	v_max_f32_e32 v2, v2, v2
	v_max_f32_e32 v1, v1, v2
	ds_swizzle_b32 v2, v1 offset:swizzle(SWAP,16)
	s_waitcnt lgkmcnt(0)
	v_max_f32_e32 v2, v2, v2
	v_max_f32_e32 v1, v1, v2
	v_mov_b32_e32 v2, v1
	s_nop 1
	v_permlane32_swap_b32_e32 v1, v2
	v_max_f32_e32 v2, v2, v2
	v_max_f32_e32 v1, v1, v1
	v_max_f32_e32 v1, v1, v2
	v_sub_f32_e32 v0, v0, v1
	v_mul_f32_e32 v0, 0x3fb8aa3b, v0
	v_exp_f32_e32 v0, v0
	s_nop 1
	v_add_f32_dpp v1, v0, v0 row_half_mirror row_mask:0xf bank_mask:0xf bound_ctrl:1
	s_nop 1
	v_add_f32_dpp v1, v1, v1 row_mirror row_mask:0xf bank_mask:0xf bound_ctrl:1
	ds_swizzle_b32 v2, v1 offset:swizzle(SWAP,16)
	s_waitcnt lgkmcnt(0)
	v_add_f32_e32 v1, v1, v2
	v_mov_b32_e32 v2, v1
	s_nop 1
	v_permlane32_swap_b32_e32 v1, v2
	s_and_saveexec_b64 s[22:23], s[8:9]
	s_cbranch_execz .LBB4_1122
	v_add_f32_e32 v1, v1, v2
	v_div_scale_f32 v2, s[42:43], v1, v1, 1.0
	v_rcp_f32_e32 v3, v2
	s_ashr_i32 s42, s18, 12
	s_ashr_i32 s43, s42, 31
	s_lshl_b64 s[42:43], s[42:43], 18
	v_fma_f32 v4, -v2, v3, 1.0
	v_fmac_f32_e32 v3, v4, v3
	v_div_scale_f32 v4, vcc, 1.0, v1, 1.0
	v_mul_f32_e32 v5, v4, v3
	v_fma_f32 v6, -v2, v5, v4
	v_fmac_f32_e32 v5, v6, v3
	v_fma_f32 v2, -v2, v5, v4
	v_div_fmas_f32 v2, v2, v3, v5
	s_add_u32 s42, s46, s42
	v_div_fixup_f32 v1, v2, v1, 1.0
	s_addc_u32 s43, s47, s43
	v_mul_f32_e32 v2, v0, v1
	v_lshl_add_u64 v[0:1], s[42:43], 0, v[56:57]
	global_store_dword v[0:1], v2, off
	s_branch .LBB4_1122
